# speedup vs baseline: 1.0140x; 1.0140x over previous
.LBB1_2:
	s_or_b64 exec, exec, s[8:9]
	s_ashr_i32 s9, s2, 3
	s_and_b32 s8, s2, 7
	s_and_b32 s9, s9, -8
	s_bfe_u32 s20, s3, 0x20006
	s_or_b32 s10, s9, s8
	s_lshl_b32 s2, s2, 4
	s_lshr_b32 s22, s3, 6
	v_bfe_u32 v1, v0, 5, 1
	s_and_b32 s2, s2, 0x380
	s_lshl_b32 s8, s20, 5
	s_ashr_i32 s11, s10, 31
	s_or_b32 s2, s8, s2
	s_lshl_b64 s[8:9], s[10:11], 19
	v_lshl_or_b32 v2, s22, 1, v1
	s_waitcnt lgkmcnt(0)
	s_cmpk_gt_u32 s3, 0xff
	s_cselect_b32 s44, s46, s44
	s_cselect_b32 s45, s47, s45
	v_and_b32_e32 v108, 0xff, v0
	v_lshlrev_b32_e32 v108, 2, v108
	global_load_dword v108, v108, s[44:45]
	s_add_u32 s14, s4, s8
	v_lshlrev_b32_e32 v6, 9, v2
	v_lshlrev_b32_e32 v2, 2, v2
	v_and_b32_e32 v5, 31, v0
	s_addc_u32 s15, s5, s9
	v_and_b32_e32 v2, 12, v2
	s_bfe_u32 s4, s3, 0x20007
	v_bitop3_b32 v2, v2, v5, s4 bitop3:0x36
	s_lshl_b32 s4, s22, 10
	v_lshl_or_b32 v192, v2, 4, v6
	s_add_i32 s21, s4, 0
	s_mov_b32 s4, m0
	s_mov_b32 m0, s21
	s_nop 0
	global_load_lds_dwordx4 v192, s[6:7]
	s_mov_b32 m0, s4
	s_add_u32 s4, s6, 0x2000
	s_addc_u32 s5, s7, 0
	s_add_i32 s31, s21, 0x2000
	s_mov_b32 s8, m0
	s_mov_b32 m0, s31
	s_nop 0
	global_load_lds_dwordx4 v192, s[4:5]
	s_mov_b32 m0, s8
	s_add_u32 s4, s6, 0x4000
	s_addc_u32 s5, s7, 0
	s_add_i32 s33, s21, 0x4000
	s_mov_b32 s8, m0
	s_mov_b32 m0, s33
	s_nop 0
	global_load_lds_dwordx4 v192, s[4:5]
	s_mov_b32 m0, s8
	s_add_u32 s4, s6, 0x6000
	s_addc_u32 s5, s7, 0
	s_add_i32 s34, s21, 0x6000
	s_mov_b32 s8, m0
	s_mov_b32 m0, s34
	s_nop 0
	global_load_lds_dwordx4 v192, s[4:5]
	s_mov_b32 m0, s8
	s_and_b32 s4, s2, 0x380
	s_lshl_b32 s4, s4, 9
	s_add_u32 s4, s14, s4
	s_addc_u32 s5, s15, 0
	s_add_i32 s27, s21, 0x10000
	s_add_i32 s28, s21, 0x12000
	s_add_i32 s29, s21, 0x14000
	s_add_i32 s30, s21, 0x16000
	s_mov_b32 s8, m0
	s_mov_b32 m0, s27
	s_nop 0
	global_load_lds_dwordx4 v192, s[4:5]
	s_mov_b32 m0, s8
	s_add_u32 s40, s4, 0x2000
	s_addc_u32 s41, s5, 0
	s_mov_b32 s8, m0
	s_mov_b32 m0, s28
	s_nop 0
	global_load_lds_dwordx4 v192, s[40:41]
	s_mov_b32 m0, s8
	s_add_u32 s40, s4, 0x4000
	s_addc_u32 s41, s5, 0
	s_mov_b32 s8, m0
	s_mov_b32 m0, s29
	s_nop 0
	global_load_lds_dwordx4 v192, s[40:41]
	s_mov_b32 m0, s8
	s_add_u32 s40, s4, 0x6000
	s_addc_u32 s41, s5, 0
	s_mov_b32 s8, m0
	s_mov_b32 m0, s30
	s_nop 0
	global_load_lds_dwordx4 v192, s[40:41]
	s_mov_b32 m0, s8
	s_add_u32 s40, s4, 0x8000
	s_addc_u32 s41, s5, 0
	s_add_i32 s42, s21, 0x18000
	s_mov_b32 s8, m0
	s_mov_b32 m0, s42
	s_nop 0
	global_load_lds_dwordx4 v192, s[40:41]
	s_mov_b32 m0, s8
	s_add_u32 s40, s4, 0xa000
	s_addc_u32 s41, s5, 0
	s_add_i32 s42, s21, 0x1a000
	s_mov_b32 s8, m0
	s_mov_b32 m0, s42
	s_nop 0
	global_load_lds_dwordx4 v192, s[40:41]
	s_mov_b32 m0, s8
	s_add_u32 s40, s4, 0xc000
	s_addc_u32 s41, s5, 0
	s_add_i32 s42, s21, 0x1c000
	s_mov_b32 s8, m0
	s_mov_b32 m0, s42
	s_nop 0
	global_load_lds_dwordx4 v192, s[40:41]
	s_mov_b32 m0, s8
	s_add_u32 s40, s4, 0xe000
	s_addc_u32 s41, s5, 0
	s_add_i32 s42, s21, 0x1e000
	s_mov_b32 s8, m0
	s_mov_b32 m0, s42
	s_nop 0
	global_load_lds_dwordx4 v192, s[40:41]
	s_mov_b32 m0, s8
	s_add_u32 s4, s6, 0x8000
	s_addc_u32 s5, s7, 0
	s_add_i32 s23, s21, 0x8000
	s_mov_b32 s8, m0
	s_mov_b32 m0, s23
	s_nop 0
	global_load_lds_dwordx4 v192, s[4:5]
	s_mov_b32 m0, s8
	s_add_u32 s4, s6, 0xa000
	s_addc_u32 s5, s7, 0
	s_add_i32 s24, s21, 0xa000
	s_mov_b32 s8, m0
	s_mov_b32 m0, s24
	s_nop 0
	global_load_lds_dwordx4 v192, s[4:5]
	s_mov_b32 m0, s8
	s_add_u32 s4, s6, 0xc000
	s_addc_u32 s5, s7, 0
	s_add_i32 s25, s21, 0xc000
	s_mov_b32 s8, m0
	s_mov_b32 m0, s25
	s_nop 0
	global_load_lds_dwordx4 v192, s[4:5]
	s_mov_b32 m0, s8
	s_add_u32 s4, s6, 0xe000
	s_addc_u32 s5, s7, 0
	s_add_i32 s26, s21, 0xe000
	s_mov_b32 s8, m0
	s_mov_b32 m0, s26
	s_nop 0
	global_load_lds_dwordx4 v192, s[4:5]
	s_mov_b32 m0, s8
	s_load_dwordx2 s[8:9], s[0:1], 0x18
	s_load_dwordx2 s[12:13], s[0:1], 0x28
	v_and_b32_e32 v81, 63, v0
	v_lshlrev_b32_e32 v2, 2, v0
	v_add_u32_e32 v6, 0x22000, v2
	s_waitcnt vmcnt(16)
	ds_write_b32 v6, v108
	s_lshr_b32 s5, s3, 8
	s_lshl_b32 s16, s20, 12
	s_lshl_b32 s4, s5, 5
	s_add_i32 s35, s16, 0
	s_add_u32 s18, s6, 0x18000
	v_and_b32_e32 v2, 12, v2
	v_bfe_u32 v0, v0, 2, 2
	s_addc_u32 s19, s7, 0
	v_bitop3_b32 v0, v2, v1, v0 bitop3:0x36
	s_add_u32 s16, s14, 0x8000
	v_lshlrev_b32_e32 v100, 4, v0
	v_or_b32_e32 v0, s4, v5
	s_addc_u32 s17, s15, 0
	s_lshl_b32 s36, s5, 7
	v_lshl_add_u32 v101, v0, 9, 0
	v_lshl_or_b32 v0, v1, 4, s36
	v_add_u32_e32 v0, 0, v0
	v_add_u32_e32 v83, v101, v100
	s_waitcnt vmcnt(4)
	s_waitcnt lgkmcnt(0)
	s_barrier
	s_lshl_b32 s40, s20, 14
	s_add_i32 s40, s40, 0x10000
	v_lshl_add_u32 v108, v5, 9, s40
	v_add_u32_e32 v109, v108, v100
	ds_read_b128 v[68:71], v109
	ds_read_b128 v[76:79], v109 offset:256
	v_xor_b32_e32 v109, 0x20, v100
	v_add_u32_e32 v109, v108, v109
	ds_read_b128 v[60:63], v109
	ds_read_b128 v[72:75], v109 offset:256
	v_xor_b32_e32 v109, 0x40, v100
	v_add_u32_e32 v109, v108, v109
	ds_read_b128 v[52:55], v109
	ds_read_b128 v[64:67], v109 offset:256
	v_xor_b32_e32 v109, 0x60, v100
	v_add_u32_e32 v109, v108, v109
	ds_read_b128 v[48:51], v109
	ds_read_b128 v[56:59], v109 offset:256
	v_xor_b32_e32 v109, 0x80, v100
	v_add_u32_e32 v109, v108, v109
	ds_read_b128 v[36:39], v109
	ds_read_b128 v[44:47], v109 offset:256
	v_xor_b32_e32 v109, 0xa0, v100
	v_add_u32_e32 v109, v108, v109
	ds_read_b128 v[28:31], v109
	ds_read_b128 v[40:43], v109 offset:256
	v_xor_b32_e32 v109, 0xc0, v100
	v_add_u32_e32 v109, v108, v109
	ds_read_b128 v[24:27], v109
	ds_read_b128 v[32:35], v109 offset:256
	v_xor_b32_e32 v109, 0xe0, v100
	v_add_u32_e32 v109, v108, v109
	ds_read_b128 v[20:23], v109
	ds_read_b128 v[16:19], v109 offset:256
	s_waitcnt vmcnt(0) lgkmcnt(0)
	s_barrier
	s_add_u32 s40, s6, 0x10000
	s_addc_u32 s41, s7, 0
	s_mov_b32 s42, m0
	s_mov_b32 m0, s27
	s_nop 0
	global_load_lds_dwordx4 v192, s[40:41]
	s_mov_b32 m0, s42
	s_add_u32 s40, s6, 0x12000
	s_addc_u32 s41, s7, 0
	s_mov_b32 s42, m0
	s_mov_b32 m0, s28
	s_nop 0
	global_load_lds_dwordx4 v192, s[40:41]
	s_mov_b32 m0, s42
	s_add_u32 s40, s6, 0x14000
	s_addc_u32 s41, s7, 0
	s_mov_b32 s42, m0
	s_mov_b32 m0, s29
	s_nop 0
	global_load_lds_dwordx4 v192, s[40:41]
	s_mov_b32 m0, s42
	s_add_u32 s40, s6, 0x16000
	s_addc_u32 s41, s7, 0
	s_mov_b32 s42, m0
	s_mov_b32 m0, s30
	s_nop 0
	global_load_lds_dwordx4 v192, s[40:41]
	s_mov_b32 m0, s42
	v_add_u32_e32 v80, 0x22000, v0
	v_lshl_add_u32 v81, v81, 4, s35
	v_add_u32_e32 v81, 0x18000, v81
	v_lshl_add_u32 v82, s5, 11, v81
	ds_read_b128 v[0:3], v80 offset:0
	ds_read_b128 v[4:7], v80 offset:32
	ds_read_b128 v[8:11], v80 offset:64
	ds_read_b128 v[12:15], v80 offset:96
	ds_read_b128 v[108:111], v80 offset:256
	ds_read_b128 v[112:115], v80 offset:288
	ds_read_b128 v[116:119], v80 offset:320
	ds_read_b128 v[120:123], v80 offset:352
	v_xor_b32_e32 v84, 0x20, v100
	v_add_u32_e32 v84, v101, v84
	v_xor_b32_e32 v85, 0x40, v100
	v_add_u32_e32 v85, v101, v85
	v_xor_b32_e32 v86, 0x60, v100
	v_add_u32_e32 v86, v101, v86
	v_xor_b32_e32 v87, 0x80, v100
	v_add_u32_e32 v87, v101, v87
	v_xor_b32_e32 v88, 0xa0, v100
	v_add_u32_e32 v88, v101, v88
	v_xor_b32_e32 v89, 0xc0, v100
	v_add_u32_e32 v89, v101, v89
	v_xor_b32_e32 v90, 0xe0, v100
	v_add_u32_e32 v90, v101, v90
	v_add_u32_e32 v208, 0x10000, v83
	v_add_u32_e32 v209, 0x10000, v84
	v_add_u32_e32 v210, 0x10000, v85
	v_add_u32_e32 v211, 0x10000, v86
	v_add_u32_e32 v212, 0x10000, v87
	v_add_u32_e32 v213, 0x10000, v88
	v_add_u32_e32 v214, 0x10000, v89
	v_add_u32_e32 v215, 0x10000, v90
	ds_read_b128 v[92:95], v83
	ds_read_b128 v[96:99], v83 offset:256
	ds_read_b128 v[200:203], v84
	ds_read_b128 v[204:207], v84 offset:256
	s_waitcnt lgkmcnt(8)
	s_waitcnt lgkmcnt(3)
	v_mfma_f32_32x32x16_bf16 v[0:15], v[92:95], v[68:71], v[0:15]
	s_waitcnt lgkmcnt(2)
	v_mfma_f32_32x32x16_bf16 v[0:15], v[96:99], v[76:79], v[0:15]
	ds_read_b128 v[92:95], v85
	ds_read_b128 v[96:99], v85 offset:256
	s_waitcnt lgkmcnt(3)
	v_mfma_f32_32x32x16_bf16 v[0:15], v[200:203], v[60:63], v[0:15]
	s_waitcnt lgkmcnt(2)
	v_mfma_f32_32x32x16_bf16 v[0:15], v[204:207], v[72:75], v[0:15]
	ds_read_b128 v[200:203], v86
	ds_read_b128 v[204:207], v86 offset:256
	s_waitcnt lgkmcnt(3)
	v_mfma_f32_32x32x16_bf16 v[0:15], v[92:95], v[52:55], v[0:15]
	s_waitcnt lgkmcnt(2)
	v_mfma_f32_32x32x16_bf16 v[0:15], v[96:99], v[64:67], v[0:15]
	ds_read_b128 v[92:95], v87
	ds_read_b128 v[96:99], v87 offset:256
	s_waitcnt lgkmcnt(3)
	v_mfma_f32_32x32x16_bf16 v[0:15], v[200:203], v[48:51], v[0:15]
	s_waitcnt lgkmcnt(2)
	v_mfma_f32_32x32x16_bf16 v[0:15], v[204:207], v[56:59], v[0:15]
	ds_read_b128 v[200:203], v88
	ds_read_b128 v[204:207], v88 offset:256
	s_waitcnt lgkmcnt(3)
	v_mfma_f32_32x32x16_bf16 v[0:15], v[92:95], v[36:39], v[0:15]
	s_waitcnt lgkmcnt(2)
	v_mfma_f32_32x32x16_bf16 v[0:15], v[96:99], v[44:47], v[0:15]
	ds_read_b128 v[92:95], v89
	ds_read_b128 v[96:99], v89 offset:256
	s_waitcnt lgkmcnt(3)
	v_mfma_f32_32x32x16_bf16 v[0:15], v[200:203], v[28:31], v[0:15]
	s_waitcnt lgkmcnt(2)
	v_mfma_f32_32x32x16_bf16 v[0:15], v[204:207], v[40:43], v[0:15]
	ds_read_b128 v[200:203], v90
	ds_read_b128 v[204:207], v90 offset:256
	s_waitcnt lgkmcnt(3)
	v_mfma_f32_32x32x16_bf16 v[0:15], v[92:95], v[24:27], v[0:15]
	s_waitcnt lgkmcnt(2)
	v_mfma_f32_32x32x16_bf16 v[0:15], v[96:99], v[32:35], v[0:15]
	ds_read_b128 v[92:95], v83 offset:32768
	ds_read_b128 v[96:99], v83 offset:33024
	s_waitcnt lgkmcnt(3)
	v_mfma_f32_32x32x16_bf16 v[0:15], v[200:203], v[20:23], v[0:15]
	s_waitcnt lgkmcnt(2)
	v_mfma_f32_32x32x16_bf16 v[0:15], v[204:207], v[16:19], v[0:15]
	ds_read_b128 v[200:203], v84 offset:32768
	ds_read_b128 v[204:207], v84 offset:33024
	s_waitcnt lgkmcnt(15)
	s_waitcnt lgkmcnt(3)
	v_mfma_f32_32x32x16_bf16 v[108:123], v[92:95], v[68:71], v[108:123]
	s_waitcnt lgkmcnt(2)
	v_mfma_f32_32x32x16_bf16 v[108:123], v[96:99], v[76:79], v[108:123]
	ds_read_b128 v[92:95], v85 offset:32768
	ds_read_b128 v[96:99], v85 offset:33024
	s_waitcnt lgkmcnt(3)
	v_mfma_f32_32x32x16_bf16 v[108:123], v[200:203], v[60:63], v[108:123]
	s_waitcnt lgkmcnt(2)
	v_mfma_f32_32x32x16_bf16 v[108:123], v[204:207], v[72:75], v[108:123]
	ds_read_b128 v[200:203], v86 offset:32768
	ds_read_b128 v[204:207], v86 offset:33024
	s_nop 1
	v_cvt_pk_bf16_f32 v216, v0, v1
	v_cvt_pk_bf16_f32 v217, v2, v3
	v_cvt_pk_bf16_f32 v218, v4, v5
	v_cvt_pk_bf16_f32 v219, v6, v7
	s_waitcnt lgkmcnt(3)
	v_mfma_f32_32x32x16_bf16 v[108:123], v[92:95], v[52:55], v[108:123]
	s_waitcnt lgkmcnt(2)
	v_mfma_f32_32x32x16_bf16 v[108:123], v[96:99], v[64:67], v[108:123]
	ds_read_b128 v[92:95], v87 offset:32768
	ds_read_b128 v[96:99], v87 offset:33024
	v_cvt_pk_bf16_f32 v220, v8, v9
	v_cvt_pk_bf16_f32 v221, v10, v11
	v_cvt_pk_bf16_f32 v222, v12, v13
	v_cvt_pk_bf16_f32 v223, v14, v15
	ds_write_b128 v82, v[216:219]
	ds_write_b128 v82, v[220:223] offset:1024
	s_waitcnt lgkmcnt(5)
	v_mfma_f32_32x32x16_bf16 v[108:123], v[200:203], v[48:51], v[108:123]
	s_waitcnt lgkmcnt(4)
	v_mfma_f32_32x32x16_bf16 v[108:123], v[204:207], v[56:59], v[108:123]
	ds_read_b128 v[200:203], v88 offset:32768
	ds_read_b128 v[204:207], v88 offset:33024
	s_waitcnt vmcnt(0)
	s_waitcnt lgkmcnt(2)
	s_barrier
	s_add_u32 s40, s6, 0x18000
	s_addc_u32 s41, s7, 0
	s_mov_b32 s42, m0
	s_mov_b32 m0, s21
	s_nop 0
	global_load_lds_dwordx4 v192, s[40:41]
	s_mov_b32 m0, s42
	s_add_u32 s40, s6, 0x1a000
	s_addc_u32 s41, s7, 0
	s_mov_b32 s42, m0
	s_mov_b32 m0, s31
	s_nop 0
	global_load_lds_dwordx4 v192, s[40:41]
	s_mov_b32 m0, s42
	s_waitcnt lgkmcnt(5)
	v_mfma_f32_32x32x16_bf16 v[108:123], v[92:95], v[36:39], v[108:123]
	s_waitcnt lgkmcnt(4)
	v_mfma_f32_32x32x16_bf16 v[108:123], v[96:99], v[44:47], v[108:123]
	ds_read_b128 v[92:95], v89 offset:32768
	ds_read_b128 v[96:99], v89 offset:33024
	s_add_u32 s40, s6, 0x1c000
	s_addc_u32 s41, s7, 0
	s_mov_b32 s42, m0
	s_mov_b32 m0, s33
	s_nop 0
	global_load_lds_dwordx4 v192, s[40:41]
	s_mov_b32 m0, s42
	s_add_u32 s40, s6, 0x1e000
	s_addc_u32 s41, s7, 0
	s_mov_b32 s42, m0
	s_mov_b32 m0, s34
	s_nop 0
	global_load_lds_dwordx4 v192, s[40:41]
	s_mov_b32 m0, s42
	ds_read_b128 v[128:131], v81
	ds_read_b128 v[132:135], v81 offset:1024
	ds_read_b128 v[136:139], v81 offset:2048
	ds_read_b128 v[140:143], v81 offset:3072
	s_waitcnt lgkmcnt(7)
	v_mfma_f32_32x32x16_bf16 v[108:123], v[200:203], v[28:31], v[108:123]
	s_waitcnt lgkmcnt(6)
	v_mfma_f32_32x32x16_bf16 v[108:123], v[204:207], v[40:43], v[108:123]
	ds_read_b128 v[200:203], v90 offset:32768
	ds_read_b128 v[204:207], v90 offset:33024
	ds_read_b128 v[0:3], v80 offset:512
	ds_read_b128 v[4:7], v80 offset:544
	ds_read_b128 v[8:11], v80 offset:576
	ds_read_b128 v[12:15], v80 offset:608
	s_waitcnt lgkmcnt(11)
	v_mfma_f32_32x32x16_bf16 v[108:123], v[92:95], v[24:27], v[108:123]
	s_waitcnt lgkmcnt(10)
	v_mfma_f32_32x32x16_bf16 v[108:123], v[96:99], v[32:35], v[108:123]
	ds_read_b128 v[92:95], v208
	ds_read_b128 v[96:99], v208 offset:256
	s_waitcnt lgkmcnt(7)
	v_mfma_f32_32x32x16_bf16 v[108:123], v[200:203], v[20:23], v[108:123]
	s_waitcnt lgkmcnt(6)
	v_mfma_f32_32x32x16_bf16 v[108:123], v[204:207], v[16:19], v[108:123]
	ds_read_b128 v[200:203], v209
	ds_read_b128 v[204:207], v209 offset:256
	s_waitcnt lgkmcnt(4)
	s_waitcnt lgkmcnt(3)
	v_mfma_f32_32x32x16_bf16 v[0:15], v[92:95], v[68:71], v[0:15]
	s_waitcnt lgkmcnt(2)
	v_mfma_f32_32x32x16_bf16 v[0:15], v[96:99], v[76:79], v[0:15]
	ds_read_b128 v[92:95], v210
	ds_read_b128 v[96:99], v210 offset:256
	s_waitcnt lgkmcnt(3)
	v_mfma_f32_32x32x16_bf16 v[0:15], v[200:203], v[60:63], v[0:15]
	s_waitcnt lgkmcnt(2)
	v_mfma_f32_32x32x16_bf16 v[0:15], v[204:207], v[72:75], v[0:15]
	ds_read_b128 v[200:203], v211
	ds_read_b128 v[204:207], v211 offset:256
	s_nop 1
	v_cvt_pk_bf16_f32 v216, v108, v109
	v_cvt_pk_bf16_f32 v217, v110, v111
	v_cvt_pk_bf16_f32 v218, v112, v113
	v_cvt_pk_bf16_f32 v219, v114, v115
	s_waitcnt lgkmcnt(3)
	v_mfma_f32_32x32x16_bf16 v[0:15], v[92:95], v[52:55], v[0:15]
	s_waitcnt lgkmcnt(2)
	v_mfma_f32_32x32x16_bf16 v[0:15], v[96:99], v[64:67], v[0:15]
	ds_read_b128 v[92:95], v212
	ds_read_b128 v[96:99], v212 offset:256
	v_cvt_pk_bf16_f32 v220, v116, v117
	v_cvt_pk_bf16_f32 v221, v118, v119
	v_cvt_pk_bf16_f32 v222, v120, v121
	v_cvt_pk_bf16_f32 v223, v122, v123
	ds_write_b128 v82, v[216:219] offset:20480
	ds_write_b128 v82, v[220:223] offset:21504
	s_waitcnt lgkmcnt(5)
	v_mfma_f32_32x32x16_bf16 v[0:15], v[200:203], v[48:51], v[0:15]
	s_waitcnt lgkmcnt(4)
	v_mfma_f32_32x32x16_bf16 v[0:15], v[204:207], v[56:59], v[0:15]
	ds_read_b128 v[200:203], v213
	ds_read_b128 v[204:207], v213 offset:256
	s_waitcnt vmcnt(0)
	s_waitcnt lgkmcnt(2)
	s_barrier
	s_add_u32 s40, s14, 0x0
	s_addc_u32 s41, s15, 0
	s_mov_b32 s42, m0
	s_mov_b32 m0, s23
	s_nop 0
	global_load_lds_dwordx4 v192, s[40:41]
	s_mov_b32 m0, s42
	s_add_u32 s40, s14, 0x2000
	s_addc_u32 s41, s15, 0
	s_mov_b32 s42, m0
	s_mov_b32 m0, s24
	s_nop 0
	global_load_lds_dwordx4 v192, s[40:41]
	s_mov_b32 m0, s42
	s_waitcnt lgkmcnt(5)
	v_mfma_f32_32x32x16_bf16 v[0:15], v[92:95], v[36:39], v[0:15]
	s_waitcnt lgkmcnt(4)
	v_mfma_f32_32x32x16_bf16 v[0:15], v[96:99], v[44:47], v[0:15]
	ds_read_b128 v[92:95], v214
	ds_read_b128 v[96:99], v214 offset:256
	s_add_u32 s40, s14, 0x4000
	s_addc_u32 s41, s15, 0
	s_mov_b32 s42, m0
	s_mov_b32 m0, s25
	s_nop 0
	global_load_lds_dwordx4 v192, s[40:41]
	s_mov_b32 m0, s42
	s_add_u32 s40, s14, 0x6000
	s_addc_u32 s41, s15, 0
	s_mov_b32 s42, m0
	s_mov_b32 m0, s26
	s_nop 0
	global_load_lds_dwordx4 v192, s[40:41]
	s_mov_b32 m0, s42
	ds_read_b128 v[144:147], v81 offset:20480
	ds_read_b128 v[148:151], v81 offset:21504
	ds_read_b128 v[152:155], v81 offset:22528
	ds_read_b128 v[156:159], v81 offset:23552
	s_waitcnt lgkmcnt(7)
	v_mfma_f32_32x32x16_bf16 v[0:15], v[200:203], v[28:31], v[0:15]
	s_waitcnt lgkmcnt(6)
	v_mfma_f32_32x32x16_bf16 v[0:15], v[204:207], v[40:43], v[0:15]
	ds_read_b128 v[200:203], v215
	ds_read_b128 v[204:207], v215 offset:256
	ds_read_b128 v[108:111], v80 offset:768
	ds_read_b128 v[112:115], v80 offset:800
	ds_read_b128 v[116:119], v80 offset:832
	ds_read_b128 v[120:123], v80 offset:864
	s_waitcnt lgkmcnt(11)
	v_mfma_f32_32x32x16_bf16 v[0:15], v[92:95], v[24:27], v[0:15]
	s_waitcnt lgkmcnt(10)
	v_mfma_f32_32x32x16_bf16 v[0:15], v[96:99], v[32:35], v[0:15]
	ds_read_b128 v[92:95], v83
	ds_read_b128 v[96:99], v83 offset:256
	s_waitcnt lgkmcnt(7)
	v_mfma_f32_32x32x16_bf16 v[0:15], v[200:203], v[20:23], v[0:15]
	s_waitcnt lgkmcnt(6)
	v_mfma_f32_32x32x16_bf16 v[0:15], v[204:207], v[16:19], v[0:15]
	ds_read_b128 v[200:203], v84
	ds_read_b128 v[204:207], v84 offset:256
	s_waitcnt lgkmcnt(4)
	s_waitcnt lgkmcnt(3)
	v_mfma_f32_32x32x16_bf16 v[108:123], v[92:95], v[68:71], v[108:123]
	s_waitcnt lgkmcnt(2)
	v_mfma_f32_32x32x16_bf16 v[108:123], v[96:99], v[76:79], v[108:123]
	ds_read_b128 v[92:95], v85
	ds_read_b128 v[96:99], v85 offset:256
	s_waitcnt lgkmcnt(3)
	v_mfma_f32_32x32x16_bf16 v[108:123], v[200:203], v[60:63], v[108:123]
	s_waitcnt lgkmcnt(2)
	v_mfma_f32_32x32x16_bf16 v[108:123], v[204:207], v[72:75], v[108:123]
	ds_read_b128 v[200:203], v86
	ds_read_b128 v[204:207], v86 offset:256
	s_nop 1
	v_cvt_pk_bf16_f32 v216, v0, v1
	v_cvt_pk_bf16_f32 v217, v2, v3
	v_cvt_pk_bf16_f32 v218, v4, v5
	v_cvt_pk_bf16_f32 v219, v6, v7
	s_waitcnt lgkmcnt(3)
	v_mfma_f32_32x32x16_bf16 v[108:123], v[92:95], v[52:55], v[108:123]
	s_waitcnt lgkmcnt(2)
	v_mfma_f32_32x32x16_bf16 v[108:123], v[96:99], v[64:67], v[108:123]
	ds_read_b128 v[92:95], v87
	ds_read_b128 v[96:99], v87 offset:256
	v_cvt_pk_bf16_f32 v220, v8, v9
	v_cvt_pk_bf16_f32 v221, v10, v11
	v_cvt_pk_bf16_f32 v222, v12, v13
	v_cvt_pk_bf16_f32 v223, v14, v15
	ds_write_b128 v82, v[216:219]
	ds_write_b128 v82, v[220:223] offset:1024
	s_waitcnt lgkmcnt(5)
	v_mfma_f32_32x32x16_bf16 v[108:123], v[200:203], v[48:51], v[108:123]
	s_waitcnt lgkmcnt(4)
	v_mfma_f32_32x32x16_bf16 v[108:123], v[204:207], v[56:59], v[108:123]
	ds_read_b128 v[200:203], v88
	ds_read_b128 v[204:207], v88 offset:256
	s_waitcnt lgkmcnt(2)
	s_barrier
	s_add_u32 s40, s14, 0x8000
	s_addc_u32 s41, s15, 0
	s_mov_b32 s42, m0
	s_mov_b32 m0, s27
	s_nop 0
	global_load_lds_dwordx4 v192, s[40:41]
	s_mov_b32 m0, s42
	s_add_u32 s40, s14, 0xa000
	s_addc_u32 s41, s15, 0
	s_mov_b32 s42, m0
	s_mov_b32 m0, s28
	s_nop 0
	global_load_lds_dwordx4 v192, s[40:41]
	s_mov_b32 m0, s42
	s_waitcnt lgkmcnt(5)
	v_mfma_f32_32x32x16_bf16 v[108:123], v[92:95], v[36:39], v[108:123]
	s_waitcnt lgkmcnt(4)
	v_mfma_f32_32x32x16_bf16 v[108:123], v[96:99], v[44:47], v[108:123]
	ds_read_b128 v[92:95], v89
	ds_read_b128 v[96:99], v89 offset:256
	s_add_u32 s40, s14, 0xc000
	s_addc_u32 s41, s15, 0
	s_mov_b32 s42, m0
	s_mov_b32 m0, s29
	s_nop 0
	global_load_lds_dwordx4 v192, s[40:41]
	s_mov_b32 m0, s42
	s_add_u32 s40, s14, 0xe000
	s_addc_u32 s41, s15, 0
	s_mov_b32 s42, m0
	s_mov_b32 m0, s30
	s_nop 0
	global_load_lds_dwordx4 v192, s[40:41]
	s_mov_b32 m0, s42
	ds_read_b128 v[160:163], v81
	ds_read_b128 v[164:167], v81 offset:1024
	ds_read_b128 v[168:171], v81 offset:2048
	ds_read_b128 v[172:175], v81 offset:3072
	s_waitcnt lgkmcnt(7)
	v_mfma_f32_32x32x16_bf16 v[108:123], v[200:203], v[28:31], v[108:123]
	s_waitcnt lgkmcnt(6)
	v_mfma_f32_32x32x16_bf16 v[108:123], v[204:207], v[40:43], v[108:123]
	ds_read_b128 v[200:203], v90
	ds_read_b128 v[204:207], v90 offset:256
	s_waitcnt lgkmcnt(7)
	v_mfma_f32_32x32x16_bf16 v[108:123], v[92:95], v[24:27], v[108:123]
	s_waitcnt lgkmcnt(6)
	v_mfma_f32_32x32x16_bf16 v[108:123], v[96:99], v[32:35], v[108:123]
	s_waitcnt lgkmcnt(1)
	v_mfma_f32_32x32x16_bf16 v[108:123], v[200:203], v[20:23], v[108:123]
	s_waitcnt lgkmcnt(0)
	v_mfma_f32_32x32x16_bf16 v[108:123], v[204:207], v[16:19], v[108:123]
	s_nop 11
	s_nop 2
	v_cvt_pk_bf16_f32 v216, v108, v109
	v_cvt_pk_bf16_f32 v217, v110, v111
	v_cvt_pk_bf16_f32 v218, v112, v113
	v_cvt_pk_bf16_f32 v219, v114, v115
	v_cvt_pk_bf16_f32 v220, v116, v117
	v_cvt_pk_bf16_f32 v221, v118, v119
	v_cvt_pk_bf16_f32 v222, v120, v121
	v_cvt_pk_bf16_f32 v223, v122, v123
	ds_write_b128 v82, v[216:219] offset:20480
	ds_write_b128 v82, v[220:223] offset:21504
	v_mbcnt_lo_u32_b32 v224, -1, 0
	v_mbcnt_hi_u32_b32 v193, -1, v224
	v_mov_b32_e32 v194, v193
	s_waitcnt vmcnt(4) lgkmcnt(0)
	s_barrier
	ds_read_b128 v[176:179], v81 offset:20480
	ds_read_b128 v[180:183], v81 offset:21504
	ds_read_b128 v[184:187], v81 offset:22528
	ds_read_b128 v[188:191], v81 offset:23552
	s_movk_i32 s7, 0x80
	s_movk_i32 s6, 0xc0
	s_mov_b32 s5, 0x10000
	s_waitcnt lgkmcnt(0)
	s_barrier
	s_cmpk_gt_u32 s3, 0xff
	s_nop 0
	v_and_b32_e32 v196, 31, v194
	v_ashrrev_i32_e32 v197, 5, v194
	v_lshlrev_b32_e32 v195, 2, v194
	v_bfe_u32 v198, v194, 2, 2
	s_cbranch_scc0 .LBB1_16
	v_lshl_add_u32 v0, s20, 2, v197
	v_lshlrev_b32_e32 v3, 2, v197
	v_add_u32_e32 v1, 2, v0
	v_lshlrev_b32_e32 v2, 9, v0
	v_and_b32_e32 v3, 12, v3
	v_bfe_u32 v0, v0, 2, 2
	v_bitop3_b32 v0, v0, v196, v3 bitop3:0x36
	v_lshl_or_b32 v199, v0, 4, v2
	v_lshlrev_b32_e32 v0, 2, v1
	s_bfe_u32 s18, s3, 0x10006
	v_and_b32_e32 v0, 12, v0
	v_bfe_u32 v2, v1, 2, 2
	v_bitop3_b32 v0, v0, v196, v2 bitop3:0x36
	v_lshrrev_b32_e32 v2, 3, v194
	s_lshl_b32 s16, s18, 8
	v_and_b32_e32 v2, 2, v2
	v_bfe_u32 v3, v194, 1, 1
	s_add_i32 s16, s16, 0
	v_lshlrev_b32_e32 v4, 3, v194
	v_lshl_add_u32 v5, v197, 11, s16
	v_bitop3_b32 v2, v2, v197, v3 bitop3:0x36
	v_and_or_b32 v4, v4, 8, v5
	v_lshlrev_b32_e32 v2, 4, v2
	v_lshlrev_b32_e32 v3, 6, v198
	v_lshl_add_u32 v4, v198, 9, v4
	v_or_b32_e32 v5, v2, v3
	v_add_u32_e32 v200, v4, v5
	v_bitop3_b32 v5, v2, v3, 32 bitop3:0xde
	v_add_u32_e32 v6, 0x1000, v4
	v_add_u32_e32 v201, v6, v5
	v_xor_b32_e32 v5, 64, v3
	v_bitop3_b32 v5, v2, v5, 32 bitop3:0xde
	v_add_u32_e32 v203, v6, v5
	v_xor_b32_e32 v5, 0x80, v3
	v_bitop3_b32 v7, v2, v3, 64 bitop3:0xf6
	v_bitop3_b32 v5, v2, v5, 32 bitop3:0xde
	v_add_u32_e32 v202, v4, v7
	v_bitop3_b32 v7, v2, v3, s7 bitop3:0xf6
	v_add_u32_e32 v205, v6, v5
	v_xor_b32_e32 v5, 0xc0, v3
	v_bitop3_b32 v3, v2, v3, s6 bitop3:0xf6
	s_and_b32 s6, s22, 2
	v_lshlrev_b32_e32 v1, 9, v1
	s_lshl_b32 s27, s6, 2
	s_lshl_b32 s7, s6, 8
	s_lshl_b32 s6, s6, 12
	v_lshl_or_b32 v208, v0, 4, v1
	s_lshl_b32 s19, s20, 11
	s_add_i32 s7, s7, 0
	s_add_i32 s6, s6, 0
	v_mov_b32_e32 v0, 0
	v_bitop3_b32 v2, v2, v5, 32 bitop3:0xde
	s_waitcnt vmcnt(0)
	s_add_i32 s19, s19, 0
	s_add_i32 s16, s7, 0x20000
	s_add_i32 s7, s7, 0x20100
	v_lshlrev_b32_e32 v209, 4, v194
	s_add_i32 s6, s6, 0x18000
	v_mov_b32_e32 v14, v0
	v_mov_b32_e32 v15, v0
	v_add_u32_e32 v204, v4, v7
	v_add_u32_e32 v206, v4, v3
	v_add_u32_e32 v207, v6, v2
	v_add_u32_e32 v212, s6, v209
	s_add_u32 s6, s8, 0xfff90000
	v_mov_b32_e32 v1, v0
	v_mov_b32_e32 v2, v0
	v_mov_b32_e32 v3, v0
	v_mov_b32_e32 v4, v0
	v_mov_b32_e32 v5, v0
	v_mov_b32_e32 v6, v0
	v_mov_b32_e32 v7, v0
	v_mov_b32_e32 v8, v0
	v_mov_b32_e32 v9, v0
	v_mov_b32_e32 v10, v0
	v_mov_b32_e32 v11, v0
	v_mov_b32_e32 v12, v0
	v_mov_b32_e32 v13, v0
	v_mov_b64_e32 v[62:63], v[14:15]
	v_mov_b64_e32 v[94:95], v[14:15]
	v_mov_b64_e32 v[126:127], v[14:15]
	v_mov_b64_e32 v[30:31], v[14:15]
	v_mov_b64_e32 v[46:47], v[14:15]
	v_mov_b64_e32 v[78:79], v[14:15]
	v_mov_b64_e32 v[110:111], v[14:15]
	v_add_u32_e32 v210, s16, v195
	v_add_u32_e32 v211, s7, v195
	s_addc_u32 s7, s9, -1
	s_mov_b32 s33, 1
	s_mov_b32 s31, 0x8000
	s_mov_b32 s29, 0x10000
	v_mov_b64_e32 v[60:61], v[12:13]
	v_mov_b64_e32 v[58:59], v[10:11]
	v_mov_b64_e32 v[56:57], v[8:9]
	v_mov_b64_e32 v[54:55], v[6:7]
	v_mov_b64_e32 v[52:53], v[4:5]
	v_mov_b64_e32 v[50:51], v[2:3]
	v_mov_b64_e32 v[48:49], v[0:1]
	v_mov_b64_e32 v[92:93], v[12:13]
	v_mov_b64_e32 v[90:91], v[10:11]
	v_mov_b64_e32 v[88:89], v[8:9]
	v_mov_b64_e32 v[86:87], v[6:7]
	v_mov_b64_e32 v[84:85], v[4:5]
	v_mov_b64_e32 v[82:83], v[2:3]
	v_mov_b64_e32 v[80:81], v[0:1]
	v_mov_b64_e32 v[124:125], v[12:13]
	v_mov_b64_e32 v[122:123], v[10:11]
	v_mov_b64_e32 v[120:121], v[8:9]
	v_mov_b64_e32 v[118:119], v[6:7]
	v_mov_b64_e32 v[116:117], v[4:5]
	v_mov_b64_e32 v[114:115], v[2:3]
	v_mov_b64_e32 v[112:113], v[0:1]
	v_mov_b64_e32 v[28:29], v[12:13]
	v_mov_b64_e32 v[26:27], v[10:11]
	v_mov_b64_e32 v[24:25], v[8:9]
	v_mov_b64_e32 v[22:23], v[6:7]
	v_mov_b64_e32 v[20:21], v[4:5]
	v_mov_b64_e32 v[18:19], v[2:3]
	v_mov_b64_e32 v[16:17], v[0:1]
	v_mov_b64_e32 v[44:45], v[12:13]
	v_mov_b64_e32 v[42:43], v[10:11]
	v_mov_b64_e32 v[40:41], v[8:9]
	v_mov_b64_e32 v[38:39], v[6:7]
	v_mov_b64_e32 v[36:37], v[4:5]
	v_mov_b64_e32 v[34:35], v[2:3]
	v_mov_b64_e32 v[32:33], v[0:1]
	v_mov_b64_e32 v[76:77], v[12:13]
	v_mov_b64_e32 v[74:75], v[10:11]
	v_mov_b64_e32 v[72:73], v[8:9]
	v_mov_b64_e32 v[70:71], v[6:7]
	v_mov_b64_e32 v[68:69], v[4:5]
	v_mov_b64_e32 v[66:67], v[2:3]
	v_mov_b64_e32 v[64:65], v[0:1]
	v_mov_b64_e32 v[108:109], v[12:13]
	v_mov_b64_e32 v[106:107], v[10:11]
	v_mov_b64_e32 v[104:105], v[8:9]
	v_mov_b64_e32 v[102:103], v[6:7]
	v_mov_b64_e32 v[100:101], v[4:5]
	v_mov_b64_e32 v[98:99], v[2:3]
	v_mov_b64_e32 v[96:97], v[0:1]
	s_waitcnt lgkmcnt(0)
	s_barrier
